# SwiGLU epilogue: 16 dead zero-initialisations of fp8 pack destinations removed
# baseline (speedup 1.0000x reference)
;     ...
;         if constexpr (FP8) { asm volatile("s_nop 15\n\ts_nop 15\n\ts_nop 15\n\ts_nop 15" ::: "memory"); }
;         E(acc, cur, wr, wc, fr, fq);
;     __device__ __forceinline__ void operator()(const f32x4 (&acc)[2][2][4][2], const Unit& u, int wr, int wc, int fr, int fq) const {
;         const int row0 = u.pm * BM + wr * 64 + fr, col0 = (u.pn & 7) * 128 + wc * 32 + 8 * fq;
;         constexpr float ds = 1.0f / (SC_W * SC_H2);
;         constexpr float c1 = -ds * LOG2E, kk = 1.0f / (ds * ds * SC_HID);
; #pragma unroll
;         for (int ai = 0; ai < 2; ++ai)
; #pragma unroll
;             for (int m = 0; m < 4; ++m) { unsigned char* rowp = HID8 + (size_t)(row0 + ai * HALF + m * 16) * D + col0;
;                 const f32x4 g0 = acc[ai][0][m][0], g1 = acc[ai][0][m][1], u0 = acc[ai][1][m][0], u1 = acc[ai][1][m][1];
;                 f32x4 t0 = g0 * c1, t1 = g1 * c1;
; #pragma unroll
;                 for (int e = 0; e < 4; ++e) { t0[e] = __builtin_amdgcn_exp2f(t0[e]); t1[e] = __builtin_amdgcn_exp2f(t1[e]); }
;                 f32x4 d0 = t0 * kk + kk, d1 = t1 * kk + kk;
; #pragma unroll
;                 for (int e = 0; e < 4; ++e) { d0[e] = __builtin_amdgcn_rcpf(d0[e]); d1[e] = __builtin_amdgcn_rcpf(d1[e]); }
;                 const f32x4 v0 = (g0 * u0) * d0, v1 = (g1 * u1) * d1;
;                 u32x2 w; w.x = pack4_fp8(v0[0], v0[1], v0[2], v0[3]); w.y = pack4_fp8(v1[0], v1[1], v1[2], v1[3]);
;                 *(u32x2*)rowp = w; }
.LBB0_1427:
	v_pk_mul_f32 v[2:3], v[152:153], s[24:25] op_sel_hi:[1,0]
	v_pk_mul_f32 v[6:7], v[150:151], s[24:25] op_sel_hi:[1,0]
	v_pk_mul_f32 v[8:9], v[148:149], s[24:25] op_sel_hi:[1,0]
	v_exp_f32_e32 v6, v6
	v_exp_f32_e32 v7, v7
	v_exp_f32_e32 v2, v2
	v_exp_f32_e32 v3, v3
	v_exp_f32_e32 v8, v8
	v_exp_f32_e32 v9, v9
	v_pk_mul_f32 v[10:11], v[146:147], s[24:25] op_sel_hi:[1,0]
	v_pk_fma_f32 v[2:3], v[2:3], s[26:27], s[26:27] op_sel_hi:[1,0,0]
	v_exp_f32_e32 v10, v10
	v_exp_f32_e32 v11, v11
	v_pk_fma_f32 v[6:7], v[6:7], s[26:27], s[26:27] op_sel_hi:[1,0,0]
	v_pk_fma_f32 v[8:9], v[8:9], s[26:27], s[26:27] op_sel_hi:[1,0,0]
	v_rcp_f32_e32 v6, v6
	v_rcp_f32_e32 v7, v7
	v_rcp_f32_e32 v2, v2
	v_rcp_f32_e32 v3, v3
	v_rcp_f32_e32 v8, v8
	v_rcp_f32_e32 v9, v9
	v_pk_fma_f32 v[10:11], v[10:11], s[26:27], s[26:27] op_sel_hi:[1,0,0]
	v_pk_mul_f32 v[12:13], v[152:153], v[160:161]
	v_rcp_f32_e32 v10, v10
	v_rcp_f32_e32 v11, v11
	v_pk_mul_f32 v[14:15], v[150:151], v[158:159]
	v_pk_mul_f32 v[2:3], v[12:13], v[2:3]
	v_pk_mul_f32 v[6:7], v[14:15], v[6:7]
	v_pk_mul_f32 v[12:13], v[148:149], v[156:157]
	v_med3_f32 v7, v7, s15, v212
	v_pk_mul_f32 v[8:9], v[12:13], v[8:9]
	v_med3_f32 v12, v6, s15, v212
	v_pk_mul_f32 v[14:15], v[146:147], v[154:155]
	v_cvt_pk_fp8_f32 v6, v12, v7
	v_pk_mul_f32 v[10:11], v[14:15], v[10:11]
	v_med3_f32 v10, v10, s15, v212
	v_med3_f32 v11, v11, s15, v212
	v_med3_f32 v2, v2, s15, v212
	v_med3_f32 v3, v3, s15, v212
	v_cvt_pk_fp8_f32 v7, v10, v11
	v_pk_mul_f32 v[10:11], v[134:135], s[24:25] op_sel_hi:[1,0]
	v_cvt_pk_fp8_f32 v6, v2, v3 op_sel:[0,0,1]
	v_med3_f32 v2, v8, s15, v212
	v_med3_f32 v3, v9, s15, v212
	v_pk_mul_f32 v[8:9], v[136:137], s[24:25] op_sel_hi:[1,0]
	v_pk_mul_f32 v[14:15], v[130:131], s[24:25] op_sel_hi:[1,0]
	v_exp_f32_e32 v10, v10
	v_exp_f32_e32 v11, v11
	v_exp_f32_e32 v14, v14
	v_exp_f32_e32 v8, v8
	v_exp_f32_e32 v9, v9
	v_exp_f32_e32 v15, v15
	v_pk_mul_f32 v[12:13], v[132:133], s[24:25] op_sel_hi:[1,0]
	v_pk_fma_f32 v[10:11], v[10:11], s[26:27], s[26:27] op_sel_hi:[1,0,0]
	v_exp_f32_e32 v12, v12
	v_exp_f32_e32 v13, v13
	v_pk_fma_f32 v[8:9], v[8:9], s[26:27], s[26:27] op_sel_hi:[1,0,0]
	v_pk_fma_f32 v[14:15], v[14:15], s[26:27], s[26:27] op_sel_hi:[1,0,0]
	v_rcp_f32_e32 v10, v10
	v_rcp_f32_e32 v11, v11
	v_rcp_f32_e32 v14, v14
	v_rcp_f32_e32 v15, v15
	v_rcp_f32_e32 v8, v8
	v_rcp_f32_e32 v9, v9
	v_lshl_add_u32 v4, s51, 8, v175
	v_pk_mul_f32 v[18:19], v[134:135], v[142:143]
	v_ashrrev_i32_e32 v5, 31, v4
	v_pk_fma_f32 v[12:13], v[12:13], s[26:27], s[26:27] op_sel_hi:[1,0,0]
	v_pk_mul_f32 v[16:17], v[136:137], v[144:145]
	v_pk_mul_f32 v[10:11], v[18:19], v[10:11]
	v_pk_mul_f32 v[18:19], v[130:131], v[138:139]
	v_cvt_pk_fp8_f32 v7, v2, v3 op_sel:[0,0,1]
	v_lshlrev_b64 v[2:3], 10, v[4:5]
	v_rcp_f32_e32 v12, v12
	v_rcp_f32_e32 v13, v13
	v_pk_mul_f32 v[8:9], v[16:17], v[8:9]
	v_pk_mul_f32 v[14:15], v[18:19], v[14:15]
	v_med3_f32 v5, v10, s15, v212
	v_med3_f32 v11, v11, s15, v212
	s_lshl_b32 s7, s50, 7
	v_readlane_b32 s10, v252, 13
	v_cvt_pk_fp8_f32 v10, v5, v11
	v_med3_f32 v5, v8, s15, v212
	v_med3_f32 v8, v9, s15, v212
	v_med3_f32 v9, v14, s15, v212
	v_med3_f32 v14, v15, s15, v212
	s_and_b32 s7, s7, 0x380
	v_readlane_b32 s11, v252, 14
	v_cvt_pk_fp8_f32 v11, v9, v14
	v_or_b32_e32 v190, s7, v169
	v_lshl_add_u64 v[2:3], s[10:11], 0, v[2:3]
	v_pk_mul_f32 v[16:17], v[132:133], v[140:141]
	v_lshl_add_u64 v[2:3], v[2:3], 0, v[190:191]
	v_pk_mul_f32 v[12:13], v[16:17], v[12:13]
	s_nop 15
	s_nop 15
	s_nop 15
	s_nop 15
	global_store_dwordx2 v[2:3], v[6:7], off
	v_or_b32_e32 v6, 16, v4
	v_cvt_pk_fp8_f32 v10, v5, v8 op_sel:[0,0,1]
	v_med3_f32 v5, v12, s15, v212
	v_med3_f32 v8, v13, s15, v212
	v_ashrrev_i32_e32 v7, 31, v6
	v_cvt_pk_fp8_f32 v11, v5, v8 op_sel:[0,0,1]
	v_lshlrev_b64 v[6:7], 10, v[6:7]
	v_lshl_add_u64 v[6:7], s[10:11], 0, v[6:7]
	v_lshl_add_u64 v[6:7], v[6:7], 0, v[190:191]
	global_store_dwordx2 v[6:7], v[10:11], off
	v_pk_mul_f32 v[10:11], v[118:119], s[24:25] op_sel_hi:[1,0]
	v_pk_mul_f32 v[8:9], v[120:121], s[24:25] op_sel_hi:[1,0]
	v_pk_mul_f32 v[14:15], v[114:115], s[24:25] op_sel_hi:[1,0]
	v_exp_f32_e32 v10, v10
	v_exp_f32_e32 v11, v11
	v_exp_f32_e32 v14, v14
	v_exp_f32_e32 v8, v8
	v_exp_f32_e32 v9, v9
	v_exp_f32_e32 v15, v15
	v_pk_mul_f32 v[12:13], v[116:117], s[24:25] op_sel_hi:[1,0]
	v_pk_fma_f32 v[10:11], v[10:11], s[26:27], s[26:27] op_sel_hi:[1,0,0]
	v_exp_f32_e32 v12, v12
	v_exp_f32_e32 v13, v13
	v_pk_fma_f32 v[8:9], v[8:9], s[26:27], s[26:27] op_sel_hi:[1,0,0]
	v_pk_fma_f32 v[14:15], v[14:15], s[26:27], s[26:27] op_sel_hi:[1,0,0]
	v_rcp_f32_e32 v10, v10
	v_rcp_f32_e32 v11, v11
	v_rcp_f32_e32 v14, v14
	v_rcp_f32_e32 v15, v15
	v_rcp_f32_e32 v8, v8
	v_rcp_f32_e32 v9, v9
	v_pk_mul_f32 v[18:19], v[118:119], v[126:127]
	v_pk_fma_f32 v[12:13], v[12:13], s[26:27], s[26:27] op_sel_hi:[1,0,0]
	v_pk_mul_f32 v[16:17], v[120:121], v[128:129]
	v_pk_mul_f32 v[10:11], v[18:19], v[10:11]
	v_pk_mul_f32 v[18:19], v[114:115], v[122:123]
	v_rcp_f32_e32 v12, v12
	v_rcp_f32_e32 v13, v13
	v_pk_mul_f32 v[8:9], v[16:17], v[8:9]
	v_pk_mul_f32 v[14:15], v[18:19], v[14:15]
	v_med3_f32 v5, v10, s15, v212
	v_med3_f32 v11, v11, s15, v212
	v_cvt_pk_fp8_f32 v10, v5, v11
	v_med3_f32 v5, v8, s15, v212
	v_med3_f32 v8, v9, s15, v212
	v_med3_f32 v9, v14, s15, v212
	v_med3_f32 v14, v15, s15, v212
	v_cvt_pk_fp8_f32 v11, v9, v14
	v_pk_mul_f32 v[16:17], v[116:117], v[124:125]
	v_or_b32_e32 v6, 32, v4
	v_pk_mul_f32 v[12:13], v[16:17], v[12:13]
	v_cvt_pk_fp8_f32 v10, v5, v8 op_sel:[0,0,1]
	v_med3_f32 v5, v12, s15, v212
	v_med3_f32 v8, v13, s15, v212
	v_ashrrev_i32_e32 v7, 31, v6
	v_cvt_pk_fp8_f32 v11, v5, v8 op_sel:[0,0,1]
	v_lshlrev_b64 v[6:7], 10, v[6:7]
;     __device__ __forceinline__ void operator()(const f32x4 (&acc)[2][2][4][2], const Unit& u, int wr, int wc, int fr, int fq) const {
;     ...
;         for (int ai = 0; ai < 2; ++ai)
; #pragma unroll
;             for (int m = 0; m < 4; ++m) { unsigned char* rowp = HID8 + (size_t)(row0 + ai * HALF + m * 16) * D + col0;
;                 const f32x4 g0 = acc[ai][0][m][0], g1 = acc[ai][0][m][1], u0 = acc[ai][1][m][0], u1 = acc[ai][1][m][1];
;                 f32x4 t0 = g0 * c1, t1 = g1 * c1;
; #pragma unroll
;                 for (int e = 0; e < 4; ++e) { t0[e] = __builtin_amdgcn_exp2f(t0[e]); t1[e] = __builtin_amdgcn_exp2f(t1[e]); }
;                 f32x4 d0 = t0 * kk + kk, d1 = t1 * kk + kk;
; #pragma unroll
;                 for (int e = 0; e < 4; ++e) { d0[e] = __builtin_amdgcn_rcpf(d0[e]); d1[e] = __builtin_amdgcn_rcpf(d1[e]); }
;                 const f32x4 v0 = (g0 * u0) * d0, v1 = (g1 * u1) * d1;
;                 u32x2 w; w.x = pack4_fp8(v0[0], v0[1], v0[2], v0[3]); w.y = pack4_fp8(v1[0], v1[1], v1[2], v1[3]);
;                 *(u32x2*)rowp = w; }
	v_lshl_add_u64 v[6:7], s[10:11], 0, v[6:7]
	v_lshl_add_u64 v[6:7], v[6:7], 0, v[190:191]
	global_store_dwordx2 v[6:7], v[10:11], off
	v_pk_mul_f32 v[6:7], v[92:93], s[24:25] op_sel_hi:[1,0]
	v_pk_mul_f32 v[8:9], v[90:91], s[24:25] op_sel_hi:[1,0]
	v_pk_mul_f32 v[10:11], v[84:85], s[24:25] op_sel_hi:[1,0]
	v_pk_mul_f32 v[12:13], v[82:83], s[24:25] op_sel_hi:[1,0]
	v_exp_f32_e32 v8, v8
	v_exp_f32_e32 v9, v9
	v_exp_f32_e32 v6, v6
	v_exp_f32_e32 v7, v7
	v_exp_f32_e32 v12, v12
	v_exp_f32_e32 v10, v10
	v_exp_f32_e32 v11, v11
	v_exp_f32_e32 v13, v13
	v_pk_fma_f32 v[6:7], v[6:7], s[26:27], s[26:27] op_sel_hi:[1,0,0]
	v_pk_fma_f32 v[8:9], v[8:9], s[26:27], s[26:27] op_sel_hi:[1,0,0]
	v_pk_fma_f32 v[10:11], v[10:11], s[26:27], s[26:27] op_sel_hi:[1,0,0]
	v_pk_fma_f32 v[12:13], v[12:13], s[26:27], s[26:27] op_sel_hi:[1,0,0]
	v_rcp_f32_e32 v8, v8
	v_rcp_f32_e32 v9, v9
	v_rcp_f32_e32 v6, v6
	v_rcp_f32_e32 v7, v7
	v_rcp_f32_e32 v12, v12
	v_rcp_f32_e32 v13, v13
	v_rcp_f32_e32 v10, v10
	v_rcp_f32_e32 v11, v11
	v_pk_mul_f32 v[14:15], v[92:93], v[104:105]
	v_pk_mul_f32 v[16:17], v[90:91], v[102:103]
	v_pk_mul_f32 v[6:7], v[14:15], v[6:7]
	v_pk_mul_f32 v[8:9], v[16:17], v[8:9]
	v_pk_mul_f32 v[14:15], v[84:85], v[100:101]
	v_pk_mul_f32 v[16:17], v[82:83], v[98:99]
	v_pk_mul_f32 v[10:11], v[14:15], v[10:11]
	v_pk_mul_f32 v[12:13], v[16:17], v[12:13]
	v_med3_f32 v14, v8, s15, v212
	v_med3_f32 v9, v9, s15, v212
	v_cvt_pk_fp8_f32 v8, v14, v9
	v_med3_f32 v12, v12, s15, v212
	v_med3_f32 v13, v13, s15, v212
	v_cvt_pk_fp8_f32 v9, v12, v13
	v_med3_f32 v6, v6, s15, v212
	v_med3_f32 v7, v7, s15, v212
	v_or_b32_e32 v4, 48, v4
	v_cvt_pk_fp8_f32 v8, v6, v7 op_sel:[0,0,1]
	v_med3_f32 v6, v10, s15, v212
	v_med3_f32 v7, v11, s15, v212
	v_ashrrev_i32_e32 v5, 31, v4
	v_cvt_pk_fp8_f32 v9, v6, v7 op_sel:[0,0,1]
	v_lshlrev_b64 v[4:5], 10, v[4:5]
	v_lshl_add_u64 v[4:5], s[10:11], 0, v[4:5]
	v_lshl_add_u64 v[4:5], v[4:5], 0, v[190:191]
	global_store_dwordx2 v[4:5], v[8:9], off
	v_pk_mul_f32 v[4:5], v[96:97], s[24:25] op_sel_hi:[1,0]
	v_pk_mul_f32 v[6:7], v[94:95], s[24:25] op_sel_hi:[1,0]
	v_pk_mul_f32 v[8:9], v[88:89], s[24:25] op_sel_hi:[1,0]
	v_pk_mul_f32 v[10:11], v[86:87], s[24:25] op_sel_hi:[1,0]
	v_exp_f32_e32 v6, v6
	v_exp_f32_e32 v7, v7
	v_exp_f32_e32 v4, v4
	v_exp_f32_e32 v5, v5
	v_exp_f32_e32 v10, v10
	v_exp_f32_e32 v8, v8
	v_exp_f32_e32 v9, v9
	v_exp_f32_e32 v11, v11
	v_pk_fma_f32 v[4:5], v[4:5], s[26:27], s[26:27] op_sel_hi:[1,0,0]
	v_pk_fma_f32 v[6:7], v[6:7], s[26:27], s[26:27] op_sel_hi:[1,0,0]
	v_pk_fma_f32 v[8:9], v[8:9], s[26:27], s[26:27] op_sel_hi:[1,0,0]
	v_pk_fma_f32 v[10:11], v[10:11], s[26:27], s[26:27] op_sel_hi:[1,0,0]
	v_rcp_f32_e32 v6, v6
	v_rcp_f32_e32 v7, v7
	v_rcp_f32_e32 v4, v4
	v_rcp_f32_e32 v5, v5
	v_rcp_f32_e32 v10, v10
	v_rcp_f32_e32 v11, v11
	v_rcp_f32_e32 v8, v8
	v_rcp_f32_e32 v9, v9
	v_pk_mul_f32 v[12:13], v[96:97], v[112:113]
	v_pk_mul_f32 v[14:15], v[94:95], v[110:111]
	v_pk_mul_f32 v[4:5], v[12:13], v[4:5]
	v_pk_mul_f32 v[6:7], v[14:15], v[6:7]
	v_pk_mul_f32 v[12:13], v[88:89], v[108:109]
	v_pk_mul_f32 v[14:15], v[86:87], v[106:107]
	v_pk_mul_f32 v[8:9], v[12:13], v[8:9]
	v_pk_mul_f32 v[10:11], v[14:15], v[10:11]
	v_med3_f32 v12, v6, s15, v212
	v_med3_f32 v7, v7, s15, v212
	v_cvt_pk_fp8_f32 v6, v12, v7
	v_med3_f32 v10, v10, s15, v212
	v_med3_f32 v11, v11, s15, v212
	v_cvt_pk_fp8_f32 v7, v10, v11
	v_med3_f32 v4, v4, s15, v212
	v_med3_f32 v5, v5, s15, v212
	v_cvt_pk_fp8_f32 v6, v4, v5 op_sel:[0,0,1]
	v_med3_f32 v4, v8, s15, v212
	v_med3_f32 v5, v9, s15, v212
	v_cvt_pk_fp8_f32 v7, v4, v5 op_sel:[0,0,1]
	s_mov_b32 s7, 0x20000
	v_add_co_u32_e32 v4, vcc, s7, v2
	v_pk_mul_f32 v[8:9], v[68:69], s[24:25] op_sel_hi:[1,0]
	s_nop 0
	v_addc_co_u32_e32 v5, vcc, 0, v3, vcc
	global_store_dwordx2 v[4:5], v[6:7], off
	v_pk_mul_f32 v[4:5], v[72:73], s[24:25] op_sel_hi:[1,0]
	v_pk_mul_f32 v[6:7], v[70:71], s[24:25] op_sel_hi:[1,0]
	v_pk_mul_f32 v[10:11], v[66:67], s[24:25] op_sel_hi:[1,0]
	v_exp_f32_e32 v6, v6
	v_exp_f32_e32 v7, v7
	v_exp_f32_e32 v4, v4
	v_exp_f32_e32 v5, v5
	v_exp_f32_e32 v10, v10
	v_exp_f32_e32 v8, v8
	v_exp_f32_e32 v9, v9
	v_exp_f32_e32 v11, v11
	v_pk_fma_f32 v[4:5], v[4:5], s[26:27], s[26:27] op_sel_hi:[1,0,0]
	v_pk_fma_f32 v[6:7], v[6:7], s[26:27], s[26:27] op_sel_hi:[1,0,0]
	v_pk_fma_f32 v[8:9], v[8:9], s[26:27], s[26:27] op_sel_hi:[1,0,0]
	v_pk_fma_f32 v[10:11], v[10:11], s[26:27], s[26:27] op_sel_hi:[1,0,0]
	v_rcp_f32_e32 v6, v6
	v_rcp_f32_e32 v7, v7
	v_rcp_f32_e32 v4, v4
	v_rcp_f32_e32 v5, v5
	v_rcp_f32_e32 v10, v10
	v_rcp_f32_e32 v11, v11
; #define PG8_BAR __builtin_amdgcn_s_barrier()
;     ...
;         if (!has_next) break;
;         cur = nxt; cA = nA; cB = nB; ++ui;
; #pragma unroll
;         for (int _h = 0; _h < 2; ++_h)
; #pragma unroll
;             for (int _i = 0; _i < 2; ++_i) cvo[_h][_i] = nvo[_h][_i];
;         if constexpr (ALIGN_EPI) { if (wr == 1) PG8_BAR; }
;     __device__ __forceinline__ void operator()(const f32x4 (&acc)[2][2][4][2], const Unit& u, int wr, int wc, int fr, int fq) const {
;     ...
;         for (int ai = 0; ai < 2; ++ai)
; #pragma unroll
;             for (int m = 0; m < 4; ++m) { unsigned char* rowp = HID8 + (size_t)(row0 + ai * HALF + m * 16) * D + col0;
;                 const f32x4 g0 = acc[ai][0][m][0], g1 = acc[ai][0][m][1], u0 = acc[ai][1][m][0], u1 = acc[ai][1][m][1];
;                 f32x4 t0 = g0 * c1, t1 = g1 * c1;
; #pragma unroll
;                 for (int e = 0; e < 4; ++e) { t0[e] = __builtin_amdgcn_exp2f(t0[e]); t1[e] = __builtin_amdgcn_exp2f(t1[e]); }
;                 f32x4 d0 = t0 * kk + kk, d1 = t1 * kk + kk;
; #pragma unroll
;                 for (int e = 0; e < 4; ++e) { d0[e] = __builtin_amdgcn_rcpf(d0[e]); d1[e] = __builtin_amdgcn_rcpf(d1[e]); }
;                 const f32x4 v0 = (g0 * u0) * d0, v1 = (g1 * u1) * d1;
;                 u32x2 w; w.x = pack4_fp8(v0[0], v0[1], v0[2], v0[3]); w.y = pack4_fp8(v1[0], v1[1], v1[2], v1[3]);
;                 *(u32x2*)rowp = w; }
	v_rcp_f32_e32 v8, v8
	v_rcp_f32_e32 v9, v9
	v_pk_mul_f32 v[12:13], v[72:73], v[80:81]
	v_pk_mul_f32 v[14:15], v[70:71], v[78:79]
	v_pk_mul_f32 v[4:5], v[12:13], v[4:5]
	v_pk_mul_f32 v[6:7], v[14:15], v[6:7]
	v_pk_mul_f32 v[12:13], v[68:69], v[76:77]
	v_pk_mul_f32 v[14:15], v[66:67], v[74:75]
	v_pk_mul_f32 v[8:9], v[12:13], v[8:9]
	v_pk_mul_f32 v[10:11], v[14:15], v[10:11]
	v_med3_f32 v12, v6, s15, v212
	v_med3_f32 v7, v7, s15, v212
	v_cvt_pk_fp8_f32 v6, v12, v7
	v_med3_f32 v10, v10, s15, v212
	v_med3_f32 v11, v11, s15, v212
	v_cvt_pk_fp8_f32 v7, v10, v11
	v_med3_f32 v4, v4, s15, v212
	v_med3_f32 v5, v5, s15, v212
	v_cvt_pk_fp8_f32 v6, v4, v5 op_sel:[0,0,1]
	v_med3_f32 v4, v8, s15, v212
	v_med3_f32 v5, v9, s15, v212
	v_cvt_pk_fp8_f32 v7, v4, v5 op_sel:[0,0,1]
	s_mov_b32 s7, 0x24000
	v_add_co_u32_e32 v4, vcc, s7, v2
	v_pk_mul_f32 v[8:9], v[52:53], s[24:25] op_sel_hi:[1,0]
	s_nop 0
	v_addc_co_u32_e32 v5, vcc, 0, v3, vcc
	global_store_dwordx2 v[4:5], v[6:7], off
	v_pk_mul_f32 v[4:5], v[56:57], s[24:25] op_sel_hi:[1,0]
	v_pk_mul_f32 v[6:7], v[54:55], s[24:25] op_sel_hi:[1,0]
	v_pk_mul_f32 v[10:11], v[50:51], s[24:25] op_sel_hi:[1,0]
	v_exp_f32_e32 v6, v6
	v_exp_f32_e32 v7, v7
	v_exp_f32_e32 v4, v4
	v_exp_f32_e32 v5, v5
	v_exp_f32_e32 v10, v10
	v_exp_f32_e32 v8, v8
	v_exp_f32_e32 v9, v9
	v_exp_f32_e32 v11, v11
	v_pk_fma_f32 v[4:5], v[4:5], s[26:27], s[26:27] op_sel_hi:[1,0,0]
	v_pk_fma_f32 v[6:7], v[6:7], s[26:27], s[26:27] op_sel_hi:[1,0,0]
	v_pk_fma_f32 v[8:9], v[8:9], s[26:27], s[26:27] op_sel_hi:[1,0,0]
	v_pk_fma_f32 v[10:11], v[10:11], s[26:27], s[26:27] op_sel_hi:[1,0,0]
	v_rcp_f32_e32 v6, v6
	v_rcp_f32_e32 v7, v7
	v_rcp_f32_e32 v4, v4
	v_rcp_f32_e32 v5, v5
	v_rcp_f32_e32 v10, v10
	v_rcp_f32_e32 v11, v11
	v_rcp_f32_e32 v8, v8
	v_rcp_f32_e32 v9, v9
	v_pk_mul_f32 v[12:13], v[56:57], v[64:65]
	v_pk_mul_f32 v[14:15], v[54:55], v[62:63]
	v_pk_mul_f32 v[4:5], v[12:13], v[4:5]
	v_pk_mul_f32 v[6:7], v[14:15], v[6:7]
	v_pk_mul_f32 v[12:13], v[52:53], v[60:61]
	v_pk_mul_f32 v[14:15], v[50:51], v[58:59]
	v_pk_mul_f32 v[8:9], v[12:13], v[8:9]
	v_pk_mul_f32 v[10:11], v[14:15], v[10:11]
	v_med3_f32 v12, v6, s15, v212
	v_med3_f32 v7, v7, s15, v212
	v_cvt_pk_fp8_f32 v6, v12, v7
	v_med3_f32 v10, v10, s15, v212
	v_med3_f32 v11, v11, s15, v212
	v_cvt_pk_fp8_f32 v7, v10, v11
	v_med3_f32 v4, v4, s15, v212
	v_med3_f32 v5, v5, s15, v212
	v_cvt_pk_fp8_f32 v6, v4, v5 op_sel:[0,0,1]
	v_med3_f32 v4, v8, s15, v212
	v_med3_f32 v5, v9, s15, v212
	v_cvt_pk_fp8_f32 v7, v4, v5 op_sel:[0,0,1]
	s_mov_b32 s7, 0x28000
	v_add_co_u32_e32 v4, vcc, s7, v2
	v_pk_mul_f32 v[8:9], v[36:37], s[24:25] op_sel_hi:[1,0]
	s_nop 0
	v_addc_co_u32_e32 v5, vcc, 0, v3, vcc
	global_store_dwordx2 v[4:5], v[6:7], off
	v_pk_mul_f32 v[4:5], v[40:41], s[24:25] op_sel_hi:[1,0]
	v_pk_mul_f32 v[6:7], v[38:39], s[24:25] op_sel_hi:[1,0]
	v_pk_mul_f32 v[10:11], v[34:35], s[24:25] op_sel_hi:[1,0]
	v_exp_f32_e32 v6, v6
	v_exp_f32_e32 v7, v7
	v_exp_f32_e32 v4, v4
	v_exp_f32_e32 v5, v5
	v_exp_f32_e32 v10, v10
	v_exp_f32_e32 v8, v8
	v_exp_f32_e32 v9, v9
	v_exp_f32_e32 v11, v11
	v_pk_fma_f32 v[4:5], v[4:5], s[26:27], s[26:27] op_sel_hi:[1,0,0]
	v_pk_fma_f32 v[6:7], v[6:7], s[26:27], s[26:27] op_sel_hi:[1,0,0]
	v_pk_fma_f32 v[8:9], v[8:9], s[26:27], s[26:27] op_sel_hi:[1,0,0]
	v_pk_fma_f32 v[10:11], v[10:11], s[26:27], s[26:27] op_sel_hi:[1,0,0]
	v_rcp_f32_e32 v6, v6
	v_rcp_f32_e32 v7, v7
	v_rcp_f32_e32 v4, v4
	v_rcp_f32_e32 v5, v5
	v_rcp_f32_e32 v10, v10
	v_rcp_f32_e32 v11, v11
	v_rcp_f32_e32 v8, v8
	v_rcp_f32_e32 v9, v9
	v_pk_mul_f32 v[12:13], v[40:41], v[48:49]
	v_pk_mul_f32 v[14:15], v[38:39], v[46:47]
	v_pk_mul_f32 v[4:5], v[12:13], v[4:5]
	v_pk_mul_f32 v[6:7], v[14:15], v[6:7]
	v_pk_mul_f32 v[12:13], v[36:37], v[44:45]
	v_pk_mul_f32 v[14:15], v[34:35], v[42:43]
	v_pk_mul_f32 v[8:9], v[12:13], v[8:9]
	v_pk_mul_f32 v[10:11], v[14:15], v[10:11]
	v_med3_f32 v12, v6, s15, v212
	v_med3_f32 v7, v7, s15, v212
	v_cvt_pk_fp8_f32 v6, v12, v7
	v_med3_f32 v10, v10, s15, v212
	v_med3_f32 v11, v11, s15, v212
	v_cvt_pk_fp8_f32 v7, v10, v11
	v_med3_f32 v4, v4, s15, v212
	v_med3_f32 v5, v5, s15, v212
	v_cvt_pk_fp8_f32 v6, v4, v5 op_sel:[0,0,1]
	v_med3_f32 v4, v8, s15, v212
	v_med3_f32 v5, v9, s15, v212
	v_cvt_pk_fp8_f32 v7, v4, v5 op_sel:[0,0,1]
	v_add_co_u32_e32 v2, vcc, 0x2c000, v2
	s_mov_b64 s[10:11], -1
	s_nop 0
	v_addc_co_u32_e32 v3, vcc, 0, v3, vcc
	s_and_b64 vcc, exec, s[36:37]
	global_store_dwordx2 v[2:3], v[6:7], off
	s_cbranch_vccnz .LBB0_1414
	s_andn2_b64 vcc, exec, s[4:5]
	s_cbranch_vccnz .LBB0_1413
	s_barrier
	s_branch .LBB0_1413
